# v23 with the fp8 W2 tiles converted in GEMM1 epilogues stored without nt (kept in L2/MALL for GEMM2 in the next phase)
# baseline (speedup 1.0000x reference)
.Lp7c_skip2:
	v_fmamk_f32 v5, v126, 0x3d000000, v14
	v_ashrrev_i32_e32 v21, 31, v20
	v_lshl_add_u64 v[18:19], s[22:23], 0, v[18:19]
	v_min_f32_e32 v5, 0x40e00000, v5
	v_lshl_add_u64 v[18:19], v[18:19], 0, v[20:21]
	v_mul_f32_e32 v23, 0xc01d265f, v5
	global_store_dwordx2 v[18:19], v[26:27], off
	v_or_b32_e32 v26, 16, v22
	v_exp_f32_e32 v23, v23
	v_ashrrev_i32_e32 v27, 31, v26
	v_cvt_pk_fp8_f32 v28, v25, v30 op_sel:[0,0,1]
	v_lshlrev_b64 v[26:27], 11, v[26:27]
	v_lshl_add_u64 v[26:27], s[22:23], 0, v[26:27]
	v_lshl_add_u64 v[26:27], v[26:27], 0, v[20:21]
	v_add_f32_e32 v23, 1.0, v23
	global_store_dwordx2 v[26:27], v[28:29], off
	v_rcp_f32_e32 v23, v23
	v_fmamk_f32 v28, v127, 0x3d000000, v16
	v_min_f32_e32 v28, 0x40e00000, v28
	v_mul_f32_e32 v29, 0xc01d265f, v28
	v_fmamk_f32 v25, v122, 0x3d000000, v24
	v_exp_f32_e32 v29, v29
	v_med3_f32 v25, v25, s73, v210
	v_mul_f32_e32 v5, v5, v23
	v_mul_f32_e32 v5, v25, v5
	v_fmamk_f32 v25, v128, 0x3d000000, v10
	v_min_f32_e32 v25, 0x40e00000, v25
	v_add_f32_e32 v23, 1.0, v29
	v_mul_f32_e32 v29, 0xc01d265f, v25
	v_rcp_f32_e32 v23, v23
	v_exp_f32_e32 v29, v29
	v_fmamk_f32 v30, v123, 0x3d000000, v15
	v_med3_f32 v30, v30, s73, v210
	v_mul_f32_e32 v23, v28, v23
	v_add_f32_e32 v28, 1.0, v29
	v_rcp_f32_e32 v28, v28
	v_mul_f32_e32 v23, v30, v23
	v_fmamk_f32 v31, v118, 0x3d000000, v6
	v_min_f32_e32 v31, 0x40e00000, v31
	v_mul_f32_e32 v25, v25, v28
	v_fmamk_f32 v28, v129, 0x3d000000, v12
	v_min_f32_e32 v28, 0x40e00000, v28
	v_mul_f32_e32 v30, 0xc01d265f, v28
	v_exp_f32_e32 v30, v30
	v_mul_f32_e32 v32, 0xc01d265f, v31
	v_fmamk_f32 v29, v124, 0x3d000000, v17
	v_exp_f32_e32 v32, v32
	v_add_f32_e32 v30, 1.0, v30
	v_rcp_f32_e32 v30, v30
	v_med3_f32 v29, v29, s73, v210
	v_mul_f32_e32 v25, v29, v25
	v_fmamk_f32 v29, v125, 0x3d000000, v13
	v_med3_f32 v29, v29, s73, v210
	v_mul_f32_e32 v28, v28, v30
	v_mul_f32_e32 v30, v29, v28
	v_add_f32_e32 v29, 1.0, v32
	v_rcp_f32_e32 v29, v29
	v_fmamk_f32 v32, v119, 0x3d000000, v8
	v_min_f32_e32 v32, 0x40e00000, v32
	v_mul_f32_e32 v33, 0xc01d265f, v32
	v_fmamk_f32 v28, v114, 0x3d000000, v11
	v_exp_f32_e32 v33, v33
	v_med3_f32 v28, v28, s73, v210
	v_mul_f32_e32 v29, v31, v29
	v_mul_f32_e32 v31, v28, v29
	v_fmamk_f32 v29, v120, 0x3d000000, v2
	v_min_f32_e32 v29, 0x40e00000, v29
	v_add_f32_e32 v28, 1.0, v33
	v_mul_f32_e32 v33, 0xc01d265f, v29
	v_rcp_f32_e32 v28, v28
	v_exp_f32_e32 v33, v33
	v_fmamk_f32 v114, v115, 0x3d000000, v7
	v_med3_f32 v114, v114, s73, v210
	v_mul_f32_e32 v28, v32, v28
	v_add_f32_e32 v32, 1.0, v33
	v_rcp_f32_e32 v32, v32
	v_mul_f32_e32 v33, v114, v28
	v_fmamk_f32 v28, v116, 0x3d000000, v9
	v_med3_f32 v28, v28, s73, v210
	v_mul_f32_e32 v29, v29, v32
	v_fmamk_f32 v32, v121, 0x3d000000, v4
	v_min_f32_e32 v32, 0x40e00000, v32
	v_mul_f32_e32 v114, 0xc01d265f, v32
	v_exp_f32_e32 v114, v114
	v_mul_f32_e32 v115, v28, v29
	v_fmamk_f32 v28, v117, 0x3d000000, v3
	v_med3_f32 v116, v28, s73, v210
	v_add_f32_e32 v28, 1.0, v114
	v_rcp_f32_e32 v114, v28
	v_mov_b32_e32 v29, v169
	v_cvt_pk_fp8_f32 v29, v31, v33
	v_mov_b32_e32 v28, v169
	v_cvt_pk_fp8_f32 v28, v5, v23
	v_mul_f32_e32 v5, v32, v114
	v_mul_f32_e32 v5, v116, v5
	v_cvt_pk_fp8_f32 v29, v115, v5 op_sel:[0,0,1]
	v_fmamk_f32 v5, v110, 0x3d000000, v14
	v_min_f32_e32 v5, 0x40e00000, v5
	v_cvt_pk_fp8_f32 v28, v25, v30 op_sel:[0,0,1]
	v_mul_f32_e32 v25, 0xc01d265f, v5
	v_or_b32_e32 v26, 32, v22
	v_exp_f32_e32 v25, v25
	v_ashrrev_i32_e32 v27, 31, v26
	v_lshlrev_b64 v[26:27], 11, v[26:27]
	v_lshl_add_u64 v[26:27], s[22:23], 0, v[26:27]
	v_lshl_add_u64 v[26:27], v[26:27], 0, v[20:21]
	v_add_f32_e32 v25, 1.0, v25
	global_store_dwordx2 v[26:27], v[28:29], off
	v_rcp_f32_e32 v25, v25
	v_fmamk_f32 v27, v111, 0x3d000000, v16
	v_min_f32_e32 v27, 0x40e00000, v27
	v_mul_f32_e32 v28, 0xc01d265f, v27
	v_fmamk_f32 v26, v106, 0x3d000000, v24
	v_exp_f32_e32 v28, v28
	v_med3_f32 v26, v26, s73, v210
	v_mul_f32_e32 v5, v5, v25
	v_mul_f32_e32 v5, v26, v5
	v_fmamk_f32 v26, v112, 0x3d000000, v10
	v_min_f32_e32 v26, 0x40e00000, v26
	v_add_f32_e32 v25, 1.0, v28
	v_mul_f32_e32 v28, 0xc01d265f, v26
	v_rcp_f32_e32 v25, v25
	v_exp_f32_e32 v28, v28
	v_fmamk_f32 v29, v107, 0x3d000000, v15
	v_med3_f32 v29, v29, s73, v210
	v_mul_f32_e32 v25, v27, v25
	v_add_f32_e32 v27, 1.0, v28
	v_rcp_f32_e32 v27, v27
	v_mul_f32_e32 v25, v29, v25
	v_fmamk_f32 v30, v102, 0x3d000000, v6
	v_min_f32_e32 v30, 0x40e00000, v30
	v_mul_f32_e32 v26, v26, v27
	v_fmamk_f32 v27, v113, 0x3d000000, v12
	v_min_f32_e32 v27, 0x40e00000, v27
	v_mul_f32_e32 v29, 0xc01d265f, v27
	v_exp_f32_e32 v29, v29
	v_mul_f32_e32 v31, 0xc01d265f, v30
	v_fmamk_f32 v28, v108, 0x3d000000, v17
	v_exp_f32_e32 v31, v31
	v_add_f32_e32 v29, 1.0, v29
	v_rcp_f32_e32 v29, v29
	v_med3_f32 v28, v28, s73, v210
	v_mul_f32_e32 v28, v28, v26
	v_fmamk_f32 v26, v109, 0x3d000000, v13
	v_med3_f32 v26, v26, s73, v210
	v_mul_f32_e32 v27, v27, v29
	v_mul_f32_e32 v29, v26, v27
	v_add_f32_e32 v27, 1.0, v31
	v_rcp_f32_e32 v27, v27
	v_fmamk_f32 v31, v103, 0x3d000000, v8
	v_min_f32_e32 v31, 0x40e00000, v31
	v_mul_f32_e32 v32, 0xc01d265f, v31
	v_fmamk_f32 v26, v98, 0x3d000000, v11
	v_exp_f32_e32 v32, v32
	v_med3_f32 v26, v26, s73, v210
	v_mul_f32_e32 v27, v30, v27
	v_mul_f32_e32 v30, v26, v27
	v_fmamk_f32 v27, v104, 0x3d000000, v2
	v_min_f32_e32 v27, 0x40e00000, v27
	v_add_f32_e32 v26, 1.0, v32
	v_mul_f32_e32 v32, 0xc01d265f, v27
	v_rcp_f32_e32 v26, v26
	v_exp_f32_e32 v32, v32
	v_fmamk_f32 v33, v99, 0x3d000000, v7
	v_med3_f32 v33, v33, s73, v210
	v_mul_f32_e32 v26, v31, v26
	v_add_f32_e32 v31, 1.0, v32
	v_rcp_f32_e32 v31, v31
	v_mul_f32_e32 v32, v33, v26
	v_fmamk_f32 v26, v100, 0x3d000000, v9
	v_med3_f32 v26, v26, s73, v210
	v_mul_f32_e32 v27, v27, v31
	v_fmamk_f32 v31, v105, 0x3d000000, v4
	v_min_f32_e32 v31, 0x40e00000, v31
	v_mul_f32_e32 v33, 0xc01d265f, v31
	v_exp_f32_e32 v33, v33
	v_mul_f32_e32 v98, v26, v27
	v_fmamk_f32 v26, v101, 0x3d000000, v3
	v_med3_f32 v99, v26, s73, v210
	v_add_f32_e32 v26, 1.0, v33
	v_rcp_f32_e32 v33, v26
	v_mov_b32_e32 v27, v169
	v_cvt_pk_fp8_f32 v27, v30, v32
	v_mov_b32_e32 v26, v169
	v_cvt_pk_fp8_f32 v26, v5, v25
	v_mul_f32_e32 v5, v31, v33
	v_mul_f32_e32 v5, v99, v5
	v_cvt_pk_fp8_f32 v27, v98, v5 op_sel:[0,0,1]
	v_fmamk_f32 v5, v94, 0x3d000000, v14
	v_min_f32_e32 v5, 0x40e00000, v5
	v_or_b32_e32 v22, 48, v22
	v_mul_f32_e32 v25, 0xc01d265f, v5
	v_ashrrev_i32_e32 v23, 31, v22
	v_cvt_pk_fp8_f32 v26, v28, v29 op_sel:[0,0,1]
	v_exp_f32_e32 v25, v25
	v_lshlrev_b64 v[22:23], 11, v[22:23]
	v_lshl_add_u64 v[22:23], s[22:23], 0, v[22:23]
	v_lshl_add_u64 v[20:21], v[22:23], 0, v[20:21]
	global_store_dwordx2 v[20:21], v[26:27], off
	v_add_f32_e32 v21, 1.0, v25
	v_fmamk_f32 v22, v95, 0x3d000000, v16
	v_rcp_f32_e32 v21, v21
	v_min_f32_e32 v22, 0x40e00000, v22
	v_mul_f32_e32 v23, 0xc01d265f, v22
	v_exp_f32_e32 v23, v23
	v_fmamk_f32 v20, v90, 0x3d000000, v24
	v_mul_f32_e32 v5, v5, v21
	v_fmamk_f32 v21, v96, 0x3d000000, v10
	v_med3_f32 v20, v20, s73, v210
	v_min_f32_e32 v21, 0x40e00000, v21
	v_mul_f32_e32 v5, v20, v5
	v_add_f32_e32 v20, 1.0, v23
	v_mul_f32_e32 v23, 0xc01d265f, v21
	v_rcp_f32_e32 v20, v20
	v_exp_f32_e32 v23, v23
	v_fmamk_f32 v25, v91, 0x3d000000, v15
	v_med3_f32 v25, v25, s73, v210
	v_mul_f32_e32 v20, v22, v20
	v_add_f32_e32 v22, 1.0, v23
	v_rcp_f32_e32 v22, v22
	v_mul_f32_e32 v23, v25, v20
	v_fmamk_f32 v20, v92, 0x3d000000, v17
	v_med3_f32 v20, v20, s73, v210
	v_mul_f32_e32 v21, v21, v22
	v_fmamk_f32 v22, v97, 0x3d000000, v12
	v_min_f32_e32 v22, 0x40e00000, v22
	v_mul_f32_e32 v25, 0xc01d265f, v22
	v_exp_f32_e32 v25, v25
	v_mul_f32_e32 v26, v20, v21
	v_fmamk_f32 v20, v93, 0x3d000000, v13
	v_med3_f32 v20, v20, s73, v210
	v_add_f32_e32 v21, 1.0, v25
	v_fmamk_f32 v25, v86, 0x3d000000, v6
	v_min_f32_e32 v25, 0x40e00000, v25
	v_rcp_f32_e32 v21, v21
	v_mul_f32_e32 v27, 0xc01d265f, v25
	v_exp_f32_e32 v27, v27
	v_fmamk_f32 v29, v83, 0x3d000000, v7
	v_mul_f32_e32 v21, v22, v21
	v_mul_f32_e32 v22, v20, v21
	v_add_f32_e32 v21, 1.0, v27
	v_rcp_f32_e32 v21, v21
	v_fmamk_f32 v27, v87, 0x3d000000, v8
	v_min_f32_e32 v27, 0x40e00000, v27
	v_mul_f32_e32 v28, 0xc01d265f, v27
	v_fmamk_f32 v20, v82, 0x3d000000, v11
	v_exp_f32_e32 v28, v28
	v_med3_f32 v20, v20, s73, v210
	v_mul_f32_e32 v21, v25, v21
	v_mul_f32_e32 v25, v20, v21
	v_fmamk_f32 v21, v88, 0x3d000000, v2
	v_min_f32_e32 v21, 0x40e00000, v21
	v_add_f32_e32 v20, 1.0, v28
	v_mul_f32_e32 v28, 0xc01d265f, v21
	v_rcp_f32_e32 v20, v20
	v_exp_f32_e32 v28, v28
	v_med3_f32 v29, v29, s73, v210
	v_mul_f32_e32 v20, v27, v20
	v_add_f32_e32 v27, 1.0, v28
	v_rcp_f32_e32 v27, v27
	v_mul_f32_e32 v28, v29, v20
	v_fmamk_f32 v20, v84, 0x3d000000, v9
	v_med3_f32 v20, v20, s73, v210
	v_mul_f32_e32 v21, v21, v27
	v_fmamk_f32 v27, v89, 0x3d000000, v4
	v_min_f32_e32 v27, 0x40e00000, v27
	v_mul_f32_e32 v29, 0xc01d265f, v27
	v_exp_f32_e32 v29, v29
	v_mul_f32_e32 v30, v20, v21
	v_fmamk_f32 v20, v85, 0x3d000000, v3
	v_med3_f32 v31, v20, s73, v210
	v_add_f32_e32 v20, 1.0, v29
	v_rcp_f32_e32 v29, v20
	v_mov_b32_e32 v21, v169
	v_cvt_pk_fp8_f32 v21, v25, v28
	v_mov_b32_e32 v20, v169
	v_cvt_pk_fp8_f32 v20, v5, v23
	v_mul_f32_e32 v5, v27, v29
	v_mul_f32_e32 v5, v31, v5
	v_cvt_pk_fp8_f32 v21, v30, v5 op_sel:[0,0,1]
	v_fmamk_f32 v5, v78, 0x3d000000, v14
	v_min_f32_e32 v5, 0x40e00000, v5
	v_cvt_pk_fp8_f32 v20, v26, v22 op_sel:[0,0,1]
	v_mul_f32_e32 v22, 0xc01d265f, v5
	v_exp_f32_e32 v25, v22
	v_add_co_u32_e32 v22, vcc, s74, v18
	v_fmamk_f32 v29, v67, 0x3d000000, v7
	s_nop 0
	v_addc_co_u32_e32 v23, vcc, 0, v19, vcc
	global_store_dwordx2 v[22:23], v[20:21], off
	v_add_f32_e32 v21, 1.0, v25
	v_fmamk_f32 v22, v79, 0x3d000000, v16
	v_rcp_f32_e32 v21, v21
	v_min_f32_e32 v22, 0x40e00000, v22
	v_mul_f32_e32 v23, 0xc01d265f, v22
	v_exp_f32_e32 v23, v23
	v_fmamk_f32 v20, v74, 0x3d000000, v24
	v_mul_f32_e32 v5, v5, v21
	v_fmamk_f32 v21, v80, 0x3d000000, v10
	v_med3_f32 v20, v20, s73, v210
	v_min_f32_e32 v21, 0x40e00000, v21
	v_mul_f32_e32 v5, v20, v5
	v_add_f32_e32 v20, 1.0, v23
	v_mul_f32_e32 v23, 0xc01d265f, v21
	v_rcp_f32_e32 v20, v20
	v_exp_f32_e32 v23, v23
	v_fmamk_f32 v25, v75, 0x3d000000, v15
	v_med3_f32 v25, v25, s73, v210
	v_mul_f32_e32 v20, v22, v20
	v_add_f32_e32 v22, 1.0, v23
	v_rcp_f32_e32 v22, v22
	v_mul_f32_e32 v23, v25, v20
	v_fmamk_f32 v20, v76, 0x3d000000, v17
	v_med3_f32 v20, v20, s73, v210
	v_mul_f32_e32 v21, v21, v22
	v_fmamk_f32 v22, v81, 0x3d000000, v12
	v_min_f32_e32 v22, 0x40e00000, v22
	v_mul_f32_e32 v25, 0xc01d265f, v22
	v_exp_f32_e32 v25, v25
	v_mul_f32_e32 v26, v20, v21
	v_fmamk_f32 v20, v77, 0x3d000000, v13
	v_med3_f32 v20, v20, s73, v210
	v_add_f32_e32 v21, 1.0, v25
	v_fmamk_f32 v25, v70, 0x3d000000, v6
	v_min_f32_e32 v25, 0x40e00000, v25
	v_rcp_f32_e32 v21, v21
	v_mul_f32_e32 v27, 0xc01d265f, v25
	v_exp_f32_e32 v27, v27
	v_med3_f32 v29, v29, s73, v210
	v_mul_f32_e32 v21, v22, v21
	v_mul_f32_e32 v22, v20, v21
	v_add_f32_e32 v21, 1.0, v27
	v_rcp_f32_e32 v21, v21
	v_fmamk_f32 v27, v71, 0x3d000000, v8
	v_min_f32_e32 v27, 0x40e00000, v27
	v_mul_f32_e32 v28, 0xc01d265f, v27
	v_fmamk_f32 v20, v66, 0x3d000000, v11
	v_exp_f32_e32 v28, v28
	v_med3_f32 v20, v20, s73, v210
	v_mul_f32_e32 v21, v25, v21
	v_mul_f32_e32 v25, v20, v21
	v_fmamk_f32 v21, v72, 0x3d000000, v2
	v_min_f32_e32 v21, 0x40e00000, v21
	v_add_f32_e32 v20, 1.0, v28
	v_mul_f32_e32 v28, 0xc01d265f, v21
	v_rcp_f32_e32 v20, v20
	v_exp_f32_e32 v28, v28
	v_mul_f32_e32 v20, v27, v20
	v_add_f32_e32 v27, 1.0, v28
	v_rcp_f32_e32 v27, v27
	v_mul_f32_e32 v28, v29, v20
	v_fmamk_f32 v20, v68, 0x3d000000, v9
	v_med3_f32 v20, v20, s73, v210
	v_mul_f32_e32 v21, v21, v27
	v_fmamk_f32 v27, v73, 0x3d000000, v4
	v_min_f32_e32 v27, 0x40e00000, v27
	v_mul_f32_e32 v29, 0xc01d265f, v27
	v_exp_f32_e32 v29, v29
	v_mul_f32_e32 v30, v20, v21
	v_fmamk_f32 v20, v69, 0x3d000000, v3
	v_med3_f32 v31, v20, s73, v210
	v_add_f32_e32 v20, 1.0, v29
	v_rcp_f32_e32 v29, v20
	v_mov_b32_e32 v21, v169
	v_cvt_pk_fp8_f32 v21, v25, v28
	v_mov_b32_e32 v20, v169
	v_cvt_pk_fp8_f32 v20, v5, v23
	v_mul_f32_e32 v5, v27, v29
	v_mul_f32_e32 v5, v31, v5
	v_cvt_pk_fp8_f32 v21, v30, v5 op_sel:[0,0,1]
	v_fmamk_f32 v5, v62, 0x3d000000, v14
	v_min_f32_e32 v5, 0x40e00000, v5
	v_cvt_pk_fp8_f32 v20, v26, v22 op_sel:[0,0,1]
	v_mul_f32_e32 v22, 0xc01d265f, v5
	v_exp_f32_e32 v25, v22
	v_add_co_u32_e32 v22, vcc, s75, v18
	v_fmamk_f32 v29, v51, 0x3d000000, v7
	s_nop 0
	v_addc_co_u32_e32 v23, vcc, 0, v19, vcc
	global_store_dwordx2 v[22:23], v[20:21], off
	v_add_f32_e32 v21, 1.0, v25
	v_fmamk_f32 v22, v63, 0x3d000000, v16
	v_rcp_f32_e32 v21, v21
	v_min_f32_e32 v22, 0x40e00000, v22
	v_mul_f32_e32 v23, 0xc01d265f, v22
	v_exp_f32_e32 v23, v23
	v_fmamk_f32 v20, v58, 0x3d000000, v24
	v_mul_f32_e32 v5, v5, v21
	v_fmamk_f32 v21, v64, 0x3d000000, v10
	v_med3_f32 v20, v20, s73, v210
	v_min_f32_e32 v21, 0x40e00000, v21
	v_mul_f32_e32 v5, v20, v5
	v_add_f32_e32 v20, 1.0, v23
	v_mul_f32_e32 v23, 0xc01d265f, v21
	v_rcp_f32_e32 v20, v20
	v_exp_f32_e32 v23, v23
	v_fmamk_f32 v25, v59, 0x3d000000, v15
	v_med3_f32 v25, v25, s73, v210
	v_mul_f32_e32 v20, v22, v20
	v_add_f32_e32 v22, 1.0, v23
	v_rcp_f32_e32 v22, v22
	v_mul_f32_e32 v23, v25, v20
	v_fmamk_f32 v20, v60, 0x3d000000, v17
	v_med3_f32 v20, v20, s73, v210
	v_mul_f32_e32 v21, v21, v22
	v_fmamk_f32 v22, v65, 0x3d000000, v12
	v_min_f32_e32 v22, 0x40e00000, v22
	v_mul_f32_e32 v25, 0xc01d265f, v22
	v_exp_f32_e32 v25, v25
	v_mul_f32_e32 v26, v20, v21
	v_fmamk_f32 v20, v61, 0x3d000000, v13
	v_med3_f32 v20, v20, s73, v210
	v_add_f32_e32 v21, 1.0, v25
	v_fmamk_f32 v25, v54, 0x3d000000, v6
	v_min_f32_e32 v25, 0x40e00000, v25
	v_rcp_f32_e32 v21, v21
	v_mul_f32_e32 v27, 0xc01d265f, v25
	v_exp_f32_e32 v27, v27
	v_med3_f32 v29, v29, s73, v210
	v_mul_f32_e32 v21, v22, v21
	v_mul_f32_e32 v22, v20, v21
	v_add_f32_e32 v21, 1.0, v27
	v_rcp_f32_e32 v21, v21
	v_fmamk_f32 v27, v55, 0x3d000000, v8
	v_min_f32_e32 v27, 0x40e00000, v27
	v_mul_f32_e32 v28, 0xc01d265f, v27
	v_fmamk_f32 v20, v50, 0x3d000000, v11
	v_exp_f32_e32 v28, v28
	v_med3_f32 v20, v20, s73, v210
	v_mul_f32_e32 v21, v25, v21
	v_mul_f32_e32 v25, v20, v21
	v_fmamk_f32 v21, v56, 0x3d000000, v2
	v_min_f32_e32 v21, 0x40e00000, v21
	v_add_f32_e32 v20, 1.0, v28
	v_mul_f32_e32 v28, 0xc01d265f, v21
	v_rcp_f32_e32 v20, v20
	v_exp_f32_e32 v28, v28
	v_fmac_f32_e32 v16, 0x3d000000, v47
	v_min_f32_e32 v16, 0x40e00000, v16
	v_mul_f32_e32 v20, v27, v20
	v_add_f32_e32 v27, 1.0, v28
	v_rcp_f32_e32 v27, v27
	v_mul_f32_e32 v28, v29, v20
	v_fmamk_f32 v20, v52, 0x3d000000, v9
	v_med3_f32 v20, v20, s73, v210
	v_mul_f32_e32 v21, v21, v27
	v_fmamk_f32 v27, v57, 0x3d000000, v4
	v_min_f32_e32 v27, 0x40e00000, v27
	v_mul_f32_e32 v29, 0xc01d265f, v27
	v_exp_f32_e32 v29, v29
	v_mul_f32_e32 v30, v20, v21
	v_fmamk_f32 v20, v53, 0x3d000000, v3
	v_med3_f32 v31, v20, s73, v210
	v_add_f32_e32 v20, 1.0, v29
	v_rcp_f32_e32 v29, v20
	v_mov_b32_e32 v21, v169
	v_cvt_pk_fp8_f32 v21, v25, v28
	v_mov_b32_e32 v20, v169
	v_cvt_pk_fp8_f32 v20, v5, v23
	v_mul_f32_e32 v5, v27, v29
	v_mul_f32_e32 v5, v31, v5
	v_cvt_pk_fp8_f32 v21, v30, v5 op_sel:[0,0,1]
	v_fmamk_f32 v5, v46, 0x3d000000, v14
	v_min_f32_e32 v5, 0x40e00000, v5
	v_mul_f32_e32 v14, 0xc01d265f, v5
	v_cvt_pk_fp8_f32 v20, v26, v22 op_sel:[0,0,1]
	v_exp_f32_e32 v14, v14
	v_add_co_u32_e32 v22, vcc, s76, v18
	v_fmamk_f32 v10, v48, 0x3d000000, v10
	s_nop 0
	v_addc_co_u32_e32 v23, vcc, 0, v19, vcc
	global_store_dwordx2 v[22:23], v[20:21], off
	v_add_f32_e32 v14, 1.0, v14
	v_mul_f32_e32 v20, 0xc01d265f, v16
	v_rcp_f32_e32 v14, v14
	v_exp_f32_e32 v20, v20
	v_min_f32_e32 v10, 0x40e00000, v10
	v_fmac_f32_e32 v12, 0x3d000000, v49
	v_mul_f32_e32 v5, v5, v14
	v_add_f32_e32 v14, 1.0, v20
	v_mul_f32_e32 v20, 0xc01d265f, v10
	v_rcp_f32_e32 v14, v14
	v_exp_f32_e32 v20, v20
	v_min_f32_e32 v12, 0x40e00000, v12
	v_fmac_f32_e32 v15, 0x3d000000, v43
	v_mul_f32_e32 v14, v16, v14
	v_add_f32_e32 v16, 1.0, v20
	v_rcp_f32_e32 v16, v16
	v_med3_f32 v15, v15, s73, v210
	v_fmac_f32_e32 v17, 0x3d000000, v44
	v_mul_f32_e32 v14, v15, v14
	v_mul_f32_e32 v10, v10, v16
	v_mul_f32_e32 v16, 0xc01d265f, v12
	v_exp_f32_e32 v16, v16
	v_med3_f32 v15, v17, s73, v210
	v_fmamk_f32 v6, v38, 0x3d000000, v6
	v_mul_f32_e32 v10, v15, v10
	v_add_f32_e32 v15, 1.0, v16
	v_min_f32_e32 v6, 0x40e00000, v6
	v_rcp_f32_e32 v15, v15
	v_mul_f32_e32 v16, 0xc01d265f, v6
	v_exp_f32_e32 v16, v16
	v_fmac_f32_e32 v13, 0x3d000000, v45
	v_med3_f32 v13, v13, s73, v210
	v_mul_f32_e32 v12, v12, v15
	v_fmac_f32_e32 v8, 0x3d000000, v39
	v_mul_f32_e32 v12, v13, v12
	v_add_f32_e32 v13, 1.0, v16
	v_min_f32_e32 v8, 0x40e00000, v8
	v_rcp_f32_e32 v13, v13
	v_mul_f32_e32 v15, 0xc01d265f, v8
	v_exp_f32_e32 v15, v15
	v_fmac_f32_e32 v11, 0x3d000000, v34
	v_fmamk_f32 v2, v40, 0x3d000000, v2
	v_med3_f32 v11, v11, s73, v210
	v_mul_f32_e32 v6, v6, v13
	v_min_f32_e32 v2, 0x40e00000, v2
	v_mul_f32_e32 v6, v11, v6
	v_add_f32_e32 v11, 1.0, v15
	v_mul_f32_e32 v13, 0xc01d265f, v2
	v_rcp_f32_e32 v11, v11
	v_exp_f32_e32 v13, v13
	v_fmac_f32_e32 v7, 0x3d000000, v35
	v_fmac_f32_e32 v4, 0x3d000000, v41
	v_med3_f32 v7, v7, s73, v210
	v_mul_f32_e32 v8, v8, v11
	v_add_f32_e32 v11, 1.0, v13
	v_fmac_f32_e32 v9, 0x3d000000, v36
	v_min_f32_e32 v4, 0x40e00000, v4
	v_rcp_f32_e32 v11, v11
	v_mul_f32_e32 v7, v7, v8
	v_med3_f32 v8, v9, s73, v210
	v_mul_f32_e32 v9, 0xc01d265f, v4
	v_exp_f32_e32 v9, v9
	v_mul_f32_e32 v2, v2, v11
	v_fmac_f32_e32 v24, 0x3d000000, v42
	v_mul_f32_e32 v8, v8, v2
	v_add_f32_e32 v2, 1.0, v9
	v_med3_f32 v21, v24, s73, v210
	v_fmac_f32_e32 v3, 0x3d000000, v37
	v_rcp_f32_e32 v9, v2
	v_mul_f32_e32 v5, v21, v5
	v_med3_f32 v11, v3, s73, v210
	v_mov_b32_e32 v2, v169
	v_mov_b32_e32 v3, v169
	v_cvt_pk_fp8_f32 v2, v5, v14
	v_cvt_pk_fp8_f32 v3, v6, v7
	v_mul_f32_e32 v4, v4, v9
	v_mul_f32_e32 v4, v11, v4
	v_cvt_pk_fp8_f32 v2, v10, v12 op_sel:[0,0,1]
	v_cvt_pk_fp8_f32 v3, v8, v4 op_sel:[0,0,1]
	v_add_co_u32_e32 v4, vcc, 0x58000, v18
	s_nop 1
	v_addc_co_u32_e32 v5, vcc, 0, v19, vcc
	s_and_b64 vcc, exec, s[4:5]
	s_mov_b64 s[4:5], -1
	global_store_dwordx2 v[4:5], v[2:3], off
	s_cmp_eq_u32 s32, 0
	s_cbranch_scc1 .Lp7c_skip3
	s_waitcnt vmcnt(8)
	v_pk_mul_f32 v[216:217], v[216:217], v[252:253]
	v_pk_mul_f32 v[218:219], v[218:219], v[252:253]
	v_pk_mul_f32 v[220:221], v[220:221], v[252:253]
	v_pk_mul_f32 v[222:223], v[222:223], v[252:253]
	v_pk_mul_f32 v[224:225], v[224:225], v[252:253]
	v_pk_mul_f32 v[226:227], v[226:227], v[252:253]
	v_pk_mul_f32 v[228:229], v[228:229], v[252:253]
	v_pk_mul_f32 v[230:231], v[230:231], v[252:253]
	v_pk_mul_f32 v[232:233], v[232:233], v[252:253]
	v_pk_mul_f32 v[234:235], v[234:235], v[252:253]
	v_pk_mul_f32 v[236:237], v[236:237], v[252:253]
	v_pk_mul_f32 v[238:239], v[238:239], v[252:253]
	v_pk_mul_f32 v[240:241], v[240:241], v[252:253]
	v_pk_mul_f32 v[242:243], v[242:243], v[252:253]
	v_pk_mul_f32 v[244:245], v[244:245], v[252:253]
	v_pk_mul_f32 v[246:247], v[246:247], v[252:253]
	v_pk_mul_f32 v[130:131], v[130:131], v[252:253]
	v_pk_mul_f32 v[132:133], v[132:133], v[252:253]
	v_pk_mul_f32 v[134:135], v[134:135], v[252:253]
	v_pk_mul_f32 v[136:137], v[136:137], v[252:253]
	v_pk_mul_f32 v[138:139], v[138:139], v[252:253]
	v_pk_mul_f32 v[140:141], v[140:141], v[252:253]
	v_pk_mul_f32 v[142:143], v[142:143], v[252:253]
	v_pk_mul_f32 v[144:145], v[144:145], v[252:253]
	v_pk_mul_f32 v[146:147], v[146:147], v[252:253]
	v_pk_mul_f32 v[148:149], v[148:149], v[252:253]
	v_pk_mul_f32 v[150:151], v[150:151], v[252:253]
	v_pk_mul_f32 v[152:153], v[152:153], v[252:253]
	v_pk_mul_f32 v[154:155], v[154:155], v[252:253]
	v_pk_mul_f32 v[156:157], v[156:157], v[252:253]
	v_pk_mul_f32 v[158:159], v[158:159], v[252:253]
	v_pk_mul_f32 v[160:161], v[160:161], v[252:253]
	v_cvt_pk_fp8_f32 v34, v216, v220
	v_cvt_pk_fp8_f32 v35, v232, v236
	v_cvt_pk_fp8_f32 v36, v130, v134
	v_cvt_pk_fp8_f32 v37, v146, v150
	v_cvt_pk_fp8_f32 v34, v224, v228 op_sel:[0,0,1]
	v_cvt_pk_fp8_f32 v35, v240, v244 op_sel:[0,0,1]
	v_cvt_pk_fp8_f32 v36, v138, v142 op_sel:[0,0,1]
	v_cvt_pk_fp8_f32 v37, v154, v158 op_sel:[0,0,1]
	v_cvt_pk_fp8_f32 v38, v217, v221
	v_cvt_pk_fp8_f32 v39, v233, v237
	v_cvt_pk_fp8_f32 v40, v131, v135
	v_cvt_pk_fp8_f32 v41, v147, v151
	v_cvt_pk_fp8_f32 v38, v225, v229 op_sel:[0,0,1]
	v_cvt_pk_fp8_f32 v39, v241, v245 op_sel:[0,0,1]
	v_cvt_pk_fp8_f32 v40, v139, v143 op_sel:[0,0,1]
	v_cvt_pk_fp8_f32 v41, v155, v159 op_sel:[0,0,1]
	v_cvt_pk_fp8_f32 v42, v218, v222
	v_cvt_pk_fp8_f32 v43, v234, v238
	v_cvt_pk_fp8_f32 v44, v132, v136
	v_cvt_pk_fp8_f32 v45, v148, v152
	v_cvt_pk_fp8_f32 v42, v226, v230 op_sel:[0,0,1]
	v_cvt_pk_fp8_f32 v43, v242, v246 op_sel:[0,0,1]
	v_cvt_pk_fp8_f32 v44, v140, v144 op_sel:[0,0,1]
	v_cvt_pk_fp8_f32 v45, v156, v160 op_sel:[0,0,1]
	v_cvt_pk_fp8_f32 v46, v219, v223
	v_cvt_pk_fp8_f32 v47, v235, v239
	v_cvt_pk_fp8_f32 v48, v133, v137
	v_cvt_pk_fp8_f32 v49, v149, v153
	v_cvt_pk_fp8_f32 v46, v227, v231 op_sel:[0,0,1]
	v_cvt_pk_fp8_f32 v47, v243, v247 op_sel:[0,0,1]
	v_cvt_pk_fp8_f32 v48, v141, v145 op_sel:[0,0,1]
	v_cvt_pk_fp8_f32 v49, v157, v161 op_sel:[0,0,1]
	s_nop 1
	ds_bpermute_b32 v50, v248, v34
	ds_bpermute_b32 v51, v248, v35
	ds_bpermute_b32 v52, v248, v36
	ds_bpermute_b32 v53, v248, v37
	ds_bpermute_b32 v54, v248, v38
	ds_bpermute_b32 v55, v248, v39
	ds_bpermute_b32 v56, v248, v40
	ds_bpermute_b32 v57, v248, v41
	ds_bpermute_b32 v58, v248, v42
	ds_bpermute_b32 v59, v248, v43
	ds_bpermute_b32 v60, v248, v44
	ds_bpermute_b32 v61, v248, v45
	ds_bpermute_b32 v62, v248, v46
	ds_bpermute_b32 v63, v248, v47
	ds_bpermute_b32 v64, v248, v48
	ds_bpermute_b32 v65, v248, v49
	s_waitcnt lgkmcnt(0)
	global_store_dwordx4 v250, v[50:53], s[88:89]
	s_add_u32 s96, s88, 0x800
	s_addc_u32 s97, s89, 0
	global_store_dwordx4 v250, v[54:57], s[96:97]
	s_add_u32 s96, s88, 0x1000
	s_addc_u32 s97, s89, 0
	global_store_dwordx4 v250, v[58:61], s[96:97]
	s_add_u32 s96, s88, 0x1800
	s_addc_u32 s97, s89, 0
	global_store_dwordx4 v250, v[62:65], s[96:97]
